# attention inner loop head pinned to a 64-byte boundary (.p2align 6), otherwise identical to the combined version
# speedup vs baseline: 1.0053x; 1.0053x over previous
.LBB0_1317:
	v_add_f32_e32 v193, 0, v154
	s_or_b32 s44, s60, 1
	s_cmp_ge_i32 s44, s71
	s_cbranch_scc1 .LBB0_1360
	s_and_b64 s[52:53], s[52:53], exec
	s_cselect_b32 s60, 3, 2
	s_ashr_i32 s45, s44, 31
	s_lshl_b64 s[52:53], s[44:45], 17
	s_add_u32 s45, s52, s46
	s_addc_u32 s59, s53, s47
	s_lshl_b64 s[52:53], s[54:55], 1
	s_add_u32 s52, s45, s52
	s_addc_u32 s53, s59, s53
	s_lshl_b32 s45, s24, 15
	s_and_b32 s45, s45, 0x18000
	v_lshl_add_u32 v66, s58, 6, v246
	v_lshl_or_b32 v166, v247, 1, s45
	v_subrev_u32_e32 v195, s75, v66
	v_lshl_add_u64 v[66:67], s[52:53], 0, v[166:167]
	s_add_i32 s52, s16, s73
	s_add_i32 s54, s58, 4
	s_ashr_i32 s53, s52, 31
	s_ashr_i32 s55, s54, 31
	s_lshl_b64 s[52:53], s[52:53], 18
	s_lshl_b64 s[58:59], s[54:55], 11
	s_add_u32 s45, s52, s58
	s_addc_u32 s53, s53, s59
	s_and_b32 s52, s74, 16
	s_or_b32 s52, s45, s52
	v_lshl_add_u64 v[220:221], v[188:189], 0, s[52:53]
	s_lshl_b64 s[52:53], s[54:55], 17
	s_add_u32 s45, s52, s46
	s_addc_u32 s52, s53, s47
	s_lshl_b64 s[50:51], s[50:51], 1
	s_add_u32 s50, s45, s50
	s_addc_u32 s51, s52, s51
	v_lshl_add_u64 v[218:219], v[208:209], 0, v[66:67]
	v_lshl_add_u64 v[222:223], v[210:211], 0, s[50:51]
	s_mov_b32 s100, m0
	s_add_i32 s93, s44, -2
	s_mul_hi_i32 s90, s93, 0x55555556
	s_mul_i32 s90, s90, 3
	s_sub_i32 s90, s93, s90
	s_mul_hi_i32 s91, s44, 0x55555556
	s_mul_i32 s91, s91, 3
	s_sub_i32 s91, s44, s91
	s_add_i32 s92, s90, s91
	s_sub_i32 s92, 3, s92
	s_add_i32 s98, s44, -1
	s_and_b32 s98, s98, 3
	s_mulk_i32 s98, 0x2800
	s_and_b32 s99, s44, 3
	s_mulk_i32 s99, 0x2800
	.p2align	6
